# mixer: packed u16 pair merge and scalar type-mask at loop top (on top of incremental output addresses)
# speedup vs baseline: 1.0020x; 1.0020x over previous
.LBB0_466:
	s_andn2_b64 s[78:79], exec, s[38:39]
	s_andn2_b64 vcc, exec, s[38:39]
	s_mov_b64 s[8:9], -1
	s_cbranch_vccnz .LBB0_468
	v_add_u32_e32 v8, s94, v106
	v_add_u32_e32 v16, s94, v105
	ds_read2st64_b32 v[2:3], v8 offset1:1
	ds_read2st64_b32 v[4:5], v8 offset0:2 offset1:3
	ds_read2st64_b32 v[6:7], v8 offset0:4 offset1:5
	ds_read2st64_b32 v[8:9], v8 offset0:6 offset1:7
	ds_read2st64_b32 v[10:11], v16 offset1:1
	ds_read2st64_b32 v[12:13], v16 offset0:2 offset1:3
	ds_read2st64_b32 v[14:15], v16 offset0:4 offset1:5
	ds_read2st64_b32 v[16:17], v16 offset0:6 offset1:7
	s_mov_b64 s[8:9], 0
	s_mov_b32 s98, 0xbfb8aa3b
	s_waitcnt lgkmcnt(4)
	v_lshlrev_b32_e32 v56, 16, v2
	v_and_b32_e32 v64, 0xffff0000, v2
	v_lshlrev_b32_e32 v57, 16, v3
	v_and_b32_e32 v65, 0xffff0000, v3
	v_lshlrev_b32_e32 v58, 16, v4
	v_and_b32_e32 v66, 0xffff0000, v4
	v_lshlrev_b32_e32 v59, 16, v5
	v_and_b32_e32 v67, 0xffff0000, v5
	v_lshlrev_b32_e32 v60, 16, v6
	v_and_b32_e32 v68, 0xffff0000, v6
	v_lshlrev_b32_e32 v61, 16, v7
	v_and_b32_e32 v69, 0xffff0000, v7
	v_lshlrev_b32_e32 v62, 16, v8
	v_and_b32_e32 v70, 0xffff0000, v8
	v_lshlrev_b32_e32 v63, 16, v9
	v_and_b32_e32 v71, 0xffff0000, v9
	v_pk_mul_f32 v[56:57], v[56:57], s[98:99] op_sel_hi:[1,0]
	v_pk_mul_f32 v[64:65], v[64:65], s[98:99] op_sel_hi:[1,0]
	v_pk_mul_f32 v[58:59], v[58:59], s[98:99] op_sel_hi:[1,0]
	v_pk_mul_f32 v[66:67], v[66:67], s[98:99] op_sel_hi:[1,0]
	v_pk_mul_f32 v[60:61], v[60:61], s[98:99] op_sel_hi:[1,0]
	v_pk_mul_f32 v[68:69], v[68:69], s[98:99] op_sel_hi:[1,0]
	v_pk_mul_f32 v[62:63], v[62:63], s[98:99] op_sel_hi:[1,0]
	v_pk_mul_f32 v[70:71], v[70:71], s[98:99] op_sel_hi:[1,0]
	v_exp_f32_e32 v56, v56
	v_exp_f32_e32 v64, v64
	v_exp_f32_e32 v57, v57
	v_exp_f32_e32 v65, v65
	v_exp_f32_e32 v58, v58
	v_exp_f32_e32 v66, v66
	v_exp_f32_e32 v59, v59
	v_exp_f32_e32 v67, v67
	v_exp_f32_e32 v60, v60
	v_exp_f32_e32 v68, v68
	v_exp_f32_e32 v61, v61
	v_exp_f32_e32 v69, v69
	v_exp_f32_e32 v62, v62
	v_exp_f32_e32 v70, v70
	v_exp_f32_e32 v63, v63
	v_exp_f32_e32 v71, v71
	s_waitcnt lgkmcnt(0)
	s_cmpk_eq_i32 s4, 0x7c0
	s_cbranch_scc1 .Lmx_qk_skip_h
	v_add_u32_e32 v176, s4, v110
	v_add_u32_e32 v177, s24, v121
	v_add_u32_e32 v178, 64, v176
	v_add_u32_e32 v179, 0x7bf, v177
	v_cndmask_b32_e64 v178, v179, v178, s[76:77]
	v_add_u32_e32 v178, s84, v178
	v_mad_i64_i32 v[178:179], s[100:101], v178, s20, v[38:39]
	s_mov_b32 m0, s19
	v_lshl_add_u64 v[180:181], v[178:179], 0, s[80:81]
	global_load_lds_dwordx4 v[180:181], off
	v_lshl_add_u64 v[178:179], v[178:179], 0, s[6:7]
	s_mov_b32 m0, s82
	v_add_u32_e32 v176, 0x44, v176
	global_load_lds_dwordx4 v[178:179], off
	v_add_u32_e32 v178, 0x7bb, v177
	v_cndmask_b32_e64 v176, v178, v176, s[76:77]
	v_add_u32_e32 v176, s84, v176
	v_mad_i64_i32 v[178:179], s[100:101], v176, s20, v[38:39]
	v_lshl_add_u64 v[180:181], v[178:179], 0, s[80:81]
	s_mov_b32 m0, s85
	v_lshl_add_u64 v[178:179], v[178:179], 0, s[6:7]
	global_load_lds_dwordx4 v[180:181], off
	s_mov_b32 m0, s86
	s_nop 0
	global_load_lds_dwordx4 v[178:179], off

.LBB0_476:
	s_waitcnt lgkmcnt(0)
	v_lshl_or_b32 v2, v149, 16, v145
	v_lshl_or_b32 v3, v150, 16, v146
	v_lshl_or_b32 v4, v151, 16, v147
	v_lshl_or_b32 v5, v152, 16, v148
	v_cvt_pk_bf16_f32 v6, v78, v79
	v_cvt_pk_bf16_f32 v7, v82, v83
	v_cvt_pk_bf16_f32 v8, v86, v87
	v_cvt_pk_bf16_f32 v9, v90, v91
	s_mov_b64 s[8:9], -1
	s_and_b64 vcc, exec, s[38:39]
	v_cvt_pk_bf16_f32 v10, v80, v81
	v_cvt_pk_bf16_f32 v11, v84, v85
	v_cvt_pk_bf16_f32 v12, v88, v89
	v_cvt_pk_bf16_f32 v13, v92, v93
	ds_write_b128 v123, v[6:9] offset:52224
	ds_write_b128 v123, v[10:13] offset:52368
	ds_write_b128 v124, v[2:5]
	s_cbranch_vccz .LBB0_478
	ds_read_b128 v[2:5], v125
	s_mov_b64 s[8:9], 0
	s_waitcnt lgkmcnt(0)
	v_pk_add_f32 v[6:7], v[4:5], 0 op_sel_hi:[1,0]
	v_pk_add_f32 v[8:9], v[2:3], 0 op_sel_hi:[1,0]
	ds_read_b128 v[2:5], v125 offset:512
	s_waitcnt lgkmcnt(0)
	v_pk_add_f32 v[6:7], v[6:7], v[4:5]
	v_pk_add_f32 v[8:9], v[8:9], v[2:3]
	ds_read_b128 v[2:5], v125 offset:1024
	s_waitcnt lgkmcnt(0)
	v_pk_add_f32 v[6:7], v[6:7], v[4:5]
	v_pk_add_f32 v[8:9], v[8:9], v[2:3]
	ds_read_b128 v[2:5], v125 offset:1536
	s_waitcnt lgkmcnt(0)
	v_pk_add_f32 v[4:5], v[6:7], v[4:5]
	v_pk_add_f32 v[2:3], v[8:9], v[2:3]
	v_exp_f32_e32 v4, v4
	v_exp_f32_e32 v2, v2
	v_exp_f32_e32 v3, v3
	v_exp_f32_e32 v5, v5
